# v69 + non-temporal hint on prep_small's converted small-weight stores (prologue phase)
# baseline (speedup 1.0000x reference)
; #define LAS __attribute__((address_space(3)))
; __device__ __forceinline__ unsigned pk2(float lo, float hi) { f32x2_cv_ v = {lo, hi}; return __builtin_bit_cast(unsigned, __builtin_convertvector(v, bf16x2_cv_)); }
; __device__ __forceinline__ void prep_item64(const float* W, int ldw, int srccol0, const float* g, bf16_t* dstrow0, int K, int k0, LAS float* scr, int lane) {
;     ...
;     for (int i = 0; i < 16; ++i) { const float gg = g ? g[k0 + 4 * i + kq] : 1.f; LAS float* d = scr + (4 * i + kq) * 65 + n4; d[0] = v[i][0] * gg; d[1] = v[i][1] * gg; d[2] = v[i][2] * gg; d[3] = v[i][3] * gg; }
;     asm volatile("s_waitcnt lgkmcnt(0)" ::: "memory");
;     const int c = lane & 7;
; #pragma unroll
;     for (int j = 0; j < 8; ++j) { const int n = (lane >> 3) + 8 * j; const LAS float* s = scr + (8 * c) * 65 + n;
;         u32x4 o; o.x = pk2(s[0 * 65], s[1 * 65]); o.y = pk2(s[2 * 65], s[3 * 65]); o.z = pk2(s[4 * 65], s[5 * 65]); o.w = pk2(s[6 * 65], s[7 * 65]);
;         *(u32x4*)(dstrow0 + (size_t)n * K + k0 + 8 * c) = o; }
;     asm volatile("s_waitcnt lgkmcnt(0)" ::: "memory");
.LBB0_7:
	s_waitcnt vmcnt(0)
	v_pk_mul_f32 v[2:3], v[2:3], v[10:11] op_sel_hi:[1,0]
	v_add_u32_e32 v6, 0x3cf0, v71
	s_ashr_i32 s39, s38, 31
	ds_write2_b32 v6, v2, v3 offset1:1
	v_pk_mul_f32 v[2:3], v[4:5], v[10:11] op_sel_hi:[1,0]
	v_add_u32_e32 v4, 0x3cf8, v71
	s_lshl_b64 s[4:5], s[38:39], 11
	ds_write2_b32 v4, v2, v3 offset1:1
	s_add_u32 s3, s68, s4
	s_waitcnt lgkmcnt(0)
	v_add_u32_e32 v26, 0x400, v115
	s_addc_u32 s36, s69, s5
	s_ashr_i32 s55, s54, 31
	ds_read2_b32 v[6:7], v115 offset0:65 offset1:73
	ds_read2_b32 v[8:9], v115 offset1:8
	ds_read2_b32 v[10:11], v115 offset0:130 offset1:138
	ds_read2_b32 v[12:13], v115 offset0:195 offset1:203
	ds_read2_b32 v[14:15], v26 offset0:4 offset1:12
	ds_read2_b32 v[16:17], v26 offset0:69 offset1:77
	ds_read2_b32 v[18:19], v26 offset0:134 offset1:142
	ds_read2_b32 v[20:21], v26 offset0:199 offset1:207
	s_lshl_b64 s[4:5], s[54:55], 1
	s_add_u32 s4, s3, s4
	s_addc_u32 s5, s36, s5
	v_lshlrev_b32_e32 v68, 1, v70
	v_lshl_add_u64 v[22:23], s[4:5], 0, v[68:69]
	s_waitcnt lgkmcnt(0)
	v_cvt_pk_bf16_f32 v2, v8, v6
	v_cvt_pk_bf16_f32 v3, v10, v12
	v_cvt_pk_bf16_f32 v4, v14, v16
	v_cvt_pk_bf16_f32 v5, v18, v20
	v_lshl_add_u64 v[24:25], v[22:23], 0, v[88:89]
	global_store_dwordx4 v[24:25], v[2:5], off nt
	s_nop 1
	v_cvt_pk_bf16_f32 v2, v9, v7
	v_cvt_pk_bf16_f32 v3, v11, v13
	v_cvt_pk_bf16_f32 v4, v15, v17
	v_cvt_pk_bf16_f32 v5, v19, v21
	ds_read2_b32 v[8:9], v115 offset0:81 offset1:89
	ds_read2_b32 v[10:11], v115 offset0:16 offset1:24
	ds_read2_b32 v[12:13], v115 offset0:146 offset1:154
	ds_read2_b32 v[14:15], v115 offset0:211 offset1:219
	ds_read2_b32 v[16:17], v26 offset0:20 offset1:28
	ds_read2_b32 v[18:19], v26 offset0:85 offset1:93
	ds_read2_b32 v[20:21], v26 offset0:150 offset1:158
	ds_read2_b32 v[24:25], v26 offset0:215 offset1:223
	v_lshl_add_u64 v[6:7], v[22:23], 0, v[90:91]
	global_store_dwordx4 v[6:7], v[2:5], off nt
	v_lshl_add_u64 v[6:7], v[22:23], 0, v[92:93]
	s_waitcnt lgkmcnt(6)
	v_cvt_pk_bf16_f32 v2, v10, v8
	s_waitcnt lgkmcnt(4)
	v_cvt_pk_bf16_f32 v3, v12, v14
	s_waitcnt lgkmcnt(2)
	v_cvt_pk_bf16_f32 v4, v16, v18
	s_waitcnt lgkmcnt(0)
	v_cvt_pk_bf16_f32 v5, v20, v24
	global_store_dwordx4 v[6:7], v[2:5], off nt
	v_lshl_add_u64 v[6:7], v[22:23], 0, v[94:95]
	s_nop 0
	v_cvt_pk_bf16_f32 v2, v11, v9
	v_cvt_pk_bf16_f32 v3, v13, v15
	v_cvt_pk_bf16_f32 v4, v17, v19
	v_cvt_pk_bf16_f32 v5, v21, v25
	ds_read2_b32 v[8:9], v115 offset0:32 offset1:40
	ds_read2_b32 v[10:11], v115 offset0:97 offset1:105
	ds_read2_b32 v[12:13], v115 offset0:162 offset1:170
	ds_read2_b32 v[14:15], v115 offset0:227 offset1:235
	ds_read2_b32 v[16:17], v26 offset0:36 offset1:44
	ds_read2_b32 v[18:19], v26 offset0:101 offset1:109
	ds_read2_b32 v[20:21], v26 offset0:166 offset1:174
	ds_read2_b32 v[24:25], v26 offset0:231 offset1:239
	global_store_dwordx4 v[6:7], v[2:5], off nt
	v_lshl_add_u64 v[6:7], v[22:23], 0, v[96:97]
	s_waitcnt lgkmcnt(6)
	v_cvt_pk_bf16_f32 v2, v8, v10
	s_waitcnt lgkmcnt(4)
	v_cvt_pk_bf16_f32 v3, v12, v14
	s_waitcnt lgkmcnt(2)
	v_cvt_pk_bf16_f32 v4, v16, v18
	s_waitcnt lgkmcnt(0)
	v_cvt_pk_bf16_f32 v5, v20, v24
	global_store_dwordx4 v[6:7], v[2:5], off nt
	v_lshl_add_u64 v[6:7], v[22:23], 0, v[98:99]
	s_nop 0
	v_cvt_pk_bf16_f32 v2, v9, v11
	v_cvt_pk_bf16_f32 v3, v13, v15
	v_cvt_pk_bf16_f32 v4, v17, v19
	v_cvt_pk_bf16_f32 v5, v21, v25
	ds_read2_b32 v[8:9], v115 offset0:48 offset1:56
	ds_read2_b32 v[10:11], v115 offset0:113 offset1:121
	ds_read2_b32 v[12:13], v115 offset0:178 offset1:186
	ds_read2_b32 v[14:15], v115 offset0:243 offset1:251
	ds_read2_b32 v[16:17], v26 offset0:52 offset1:60
	ds_read2_b32 v[18:19], v26 offset0:117 offset1:125
	ds_read2_b32 v[20:21], v26 offset0:182 offset1:190
	ds_read2_b32 v[24:25], v26 offset0:247 offset1:255
	global_store_dwordx4 v[6:7], v[2:5], off nt
	v_lshl_add_u64 v[6:7], v[22:23], 0, v[100:101]
	s_waitcnt lgkmcnt(6)
	v_cvt_pk_bf16_f32 v2, v8, v10
	s_waitcnt lgkmcnt(4)
	v_cvt_pk_bf16_f32 v3, v12, v14
	s_waitcnt lgkmcnt(2)
	v_cvt_pk_bf16_f32 v4, v16, v18
	s_waitcnt lgkmcnt(0)
	v_cvt_pk_bf16_f32 v5, v20, v24
	global_store_dwordx4 v[6:7], v[2:5], off nt
	v_lshl_add_u64 v[6:7], v[22:23], 0, v[102:103]
	s_nop 0
	v_cvt_pk_bf16_f32 v2, v9, v11
	v_cvt_pk_bf16_f32 v3, v13, v15
	v_cvt_pk_bf16_f32 v4, v17, v19
	v_cvt_pk_bf16_f32 v5, v21, v25
	global_store_dwordx4 v[6:7], v[2:5], off nt
	s_waitcnt lgkmcnt(0)

; __device__ __forceinline__ void prep_item64(const float* W, int ldw, int srccol0, const float* g, bf16_t* dstrow0, int K, int k0, LAS float* scr, int lane) {
;     f32x4 v[16];
;     const int kq = lane >> 4, n4 = (lane & 15) * 4;
; #pragma unroll
;     for (int i = 0; i < 16; ++i) v[i] = __builtin_nontemporal_load((const f32x4*)(W + (size_t)(k0 + 4 * i + kq) * ldw + srccol0 + n4));
; #pragma unroll
;     for (int i = 0; i < 16; ++i) { const float gg = g ? g[k0 + 4 * i + kq] : 1.f; LAS float* d = scr + (4 * i + kq) * 65 + n4; d[0] = v[i][0] * gg; d[1] = v[i][1] * gg; d[2] = v[i][2] * gg; d[3] = v[i][3] * gg; }
;     asm volatile("s_waitcnt lgkmcnt(0)" ::: "memory");
;     const int c = lane & 7;
; #pragma unroll
;     for (int j = 0; j < 8; ++j) { const int n = (lane >> 3) + 8 * j; const LAS float* s = scr + (8 * c) * 65 + n;
;         u32x4 o; o.x = pk2(s[0 * 65], s[1 * 65]); o.y = pk2(s[2 * 65], s[3 * 65]); o.z = pk2(s[4 * 65], s[5 * 65]); o.w = pk2(s[6 * 65], s[7 * 65]);
;         *(u32x4*)(dstrow0 + (size_t)n * K + k0 + 8 * c) = o; }
;     asm volatile("s_waitcnt lgkmcnt(0)" ::: "memory");
; }
; __device__ __forceinline__ void phase_prep_small(Frame& F) {
;     const Params& P = *F.P;
;     LAS float* scr = (LAS float*)(F.lds + F.wave * 16640);
;     constexpr int I_IN = 16 * 34, I_INT = 16 * 4, I_UQ = 6 * 12, I_UKV = 4 * 16, I_OUT = 16 * 16, I_PG = 16 * 16, I_PE = 4 * 16, I_L = I_IN + I_INT + I_UQ + I_UKV + I_OUT + I_PG + I_PE;
;     for (int it = F.gw(); it < NLAYER * I_L; it += F.ngw()) {
;         const int l = it / I_L; int r = it % I_L;
;         unsigned char* wb = F.ws + WS_WSM + (size_t)l * WSM_STRIDE;
;         if (r < I_IN) { const int kb = r / 34, n0 = (r % 34) * 64; int src;
;             if (n0 < 1536) src = n0; else if (n0 < 1792) src = 1920 + (n0 - 1536); else src = 1536 + (n0 - 1792);
;             prep_item64(P.in[4] + (size_t)l * DM * INC, INC, src, P.in[3] + l * DM, (bf16_t*)(wb + WSM_IN) + (size_t)n0 * DM, DM, kb * 64, scr, F.lane); continue; }
;         r -= I_IN;
;         if (r < I_INT) { const int kb = r / 4, n0 = 2176 + (r % 4) * 32; const int src = n0 < 2208 ? n0 : -1;
;             prep_item(P.in[4] + (size_t)l * DM * INC, INC, src, P.in[3] + l * DM, (bf16_t*)(wb + WSM_IN) + (size_t)n0 * DM, DM, kb * 64, scr, F.lane); continue; }
;         r -= I_INT;
;         if (r < I_UQ) { const int kb = r / 12, n0 = (r % 12) * 64;
.LBB0_11:
	s_cmpk_gt_u32 s70, 0x25f
	s_cbranch_scc0 .LBB0_125
	s_cmpk_gt_u32 s70, 0x2a7
	s_cbranch_scc0 .LBB0_98
	s_cmpk_gt_u32 s70, 0x2e7
	s_cbranch_scc0 .LBB0_71
	s_cmpk_gt_u32 s70, 0x3e7
	s_cbranch_scc0 .LBB0_44
	s_cmpk_gt_u32 s70, 0x4e7
	s_cbranch_scc0 .LBB0_17
	s_add_i32 s3, s70, 0xfffffb18
	s_lshl_b32 s4, s3, 6
	s_and_b32 s36, s4, 0x3c0
	s_lshl_b64 s[4:5], s[54:55], 20
	s_add_u32 s4, s6, s4
	s_addc_u32 s5, s7, s5
	s_lshl_b32 s38, s36, 9
	s_add_u32 s38, s68, s38
	s_addc_u32 s39, s69, 0
	s_lshl_b32 s3, s3, 2
	s_and_b32 s3, s3, 0x7fffffc0
	s_lshl_b32 s36, s36, 2
	s_add_u32 s4, s4, s36
	v_or_b32_e32 v62, s3, v67
	s_addc_u32 s5, s5, 0
	v_lshlrev_b32_e32 v68, 2, v66
	v_lshl_add_u64 v[64:65], s[4:5], 0, v[68:69]
	v_or_b32_e32 v68, 4, v62
	v_lshlrev_b64 v[4:5], 12, v[68:69]
	v_or_b32_e32 v68, 8, v62
	v_mov_b32_e32 v63, v69
	v_lshlrev_b64 v[10:11], 12, v[68:69]
	v_or_b32_e32 v68, 12, v62
	v_lshlrev_b64 v[2:3], 12, v[62:63]
	v_lshlrev_b64 v[12:13], 12, v[68:69]
	v_or_b32_e32 v68, 16, v62
	v_lshl_add_u64 v[2:3], v[64:65], 0, v[2:3]
	v_lshl_add_u64 v[6:7], v[64:65], 0, v[4:5]
	v_lshl_add_u64 v[10:11], v[64:65], 0, v[10:11]
	v_lshl_add_u64 v[14:15], v[64:65], 0, v[12:13]
	v_lshlrev_b64 v[18:19], 12, v[68:69]
	v_or_b32_e32 v68, 20, v62
	global_load_dwordx4 v[2:5], v[2:3], off nt
	s_nop 0
	global_load_dwordx4 v[6:9], v[6:7], off nt
	s_nop 0
	global_load_dwordx4 v[10:13], v[10:11], off nt
	s_nop 0
	global_load_dwordx4 v[14:17], v[14:15], off nt
	v_lshl_add_u64 v[18:19], v[64:65], 0, v[18:19]
	v_lshlrev_b64 v[22:23], 12, v[68:69]
	global_load_dwordx4 v[18:21], v[18:19], off nt
	v_lshl_add_u64 v[22:23], v[64:65], 0, v[22:23]
	v_or_b32_e32 v68, 24, v62
	global_load_dwordx4 v[22:25], v[22:23], off nt
	v_lshlrev_b64 v[26:27], 12, v[68:69]
	v_lshl_add_u64 v[26:27], v[64:65], 0, v[26:27]
	v_or_b32_e32 v68, 28, v62
	global_load_dwordx4 v[26:29], v[26:27], off nt
	v_lshlrev_b64 v[30:31], 12, v[68:69]
	v_lshl_add_u64 v[30:31], v[64:65], 0, v[30:31]
	v_or_b32_e32 v68, 32, v62
	global_load_dwordx4 v[30:33], v[30:31], off nt
	v_lshlrev_b64 v[34:35], 12, v[68:69]
	v_lshl_add_u64 v[34:35], v[64:65], 0, v[34:35]
	v_or_b32_e32 v68, 36, v62
	global_load_dwordx4 v[34:37], v[34:35], off nt
	v_lshlrev_b64 v[38:39], 12, v[68:69]
	v_lshl_add_u64 v[38:39], v[64:65], 0, v[38:39]
	v_or_b32_e32 v68, 40, v62
	global_load_dwordx4 v[38:41], v[38:39], off nt
	v_lshlrev_b64 v[42:43], 12, v[68:69]
	v_lshl_add_u64 v[42:43], v[64:65], 0, v[42:43]
	v_or_b32_e32 v68, 44, v62
	global_load_dwordx4 v[42:45], v[42:43], off nt
	v_lshlrev_b64 v[46:47], 12, v[68:69]
	v_lshl_add_u64 v[46:47], v[64:65], 0, v[46:47]
	v_or_b32_e32 v68, 48, v62
	global_load_dwordx4 v[46:49], v[46:47], off nt
	v_lshlrev_b64 v[50:51], 12, v[68:69]
	v_lshl_add_u64 v[50:51], v[64:65], 0, v[50:51]
	v_or_b32_e32 v68, 52, v62
	global_load_dwordx4 v[50:53], v[50:51], off nt
	v_lshlrev_b64 v[54:55], 12, v[68:69]
	v_lshl_add_u64 v[54:55], v[64:65], 0, v[54:55]
	v_or_b32_e32 v68, 56, v62
	global_load_dwordx4 v[54:57], v[54:55], off nt
	v_lshlrev_b64 v[58:59], 12, v[68:69]
	v_lshl_add_u64 v[58:59], v[64:65], 0, v[58:59]
	v_or_b32_e32 v68, 60, v62
	global_load_dwordx4 v[58:61], v[58:59], off nt
	v_lshlrev_b64 v[62:63], 12, v[68:69]
	v_lshl_add_u64 v[62:63], v[64:65], 0, v[62:63]
	global_load_dwordx4 v[62:65], v[62:63], off nt
	v_add_u32_e32 v68, 0x410, v71
	v_add_u32_e32 v120, 0x418, v71
	v_add_u32_e32 v121, 0x820, v71
	v_add_u32_e32 v131, 0x828, v71
	v_add_u32_e32 v132, 0xc30, v71
	v_add_u32_e32 v133, 0xc38, v71
	v_add_u32_e32 v134, 0x1040, v71
	s_lshl_b32 s3, s3, 1
	s_add_u32 s4, s38, s3
	s_addc_u32 s5, s39, 0
	s_waitcnt vmcnt(15)
	ds_write2_b32 v71, v2, v3 offset1:1
	ds_write2_b32 v71, v4, v5 offset0:2 offset1:3
	s_waitcnt vmcnt(14)
	ds_write2_b32 v68, v6, v7 offset1:1
	ds_write2_b32 v120, v8, v9 offset1:1
	s_waitcnt vmcnt(13)
	ds_write2_b32 v121, v10, v11 offset1:1
	ds_write2_b32 v131, v12, v13 offset1:1
	s_waitcnt vmcnt(12)
	ds_write2_b32 v132, v14, v15 offset1:1
	ds_write2_b32 v133, v16, v17 offset1:1
	s_waitcnt vmcnt(11)
	ds_write2_b32 v134, v18, v19 offset1:1
	v_add_u32_e32 v2, 0x1048, v71
	v_lshlrev_b32_e32 v68, 1, v70
	ds_write2_b32 v2, v20, v21 offset1:1
	v_add_u32_e32 v2, 0x1450, v71
	s_waitcnt vmcnt(10)
	ds_write2_b32 v2, v22, v23 offset1:1
	v_add_u32_e32 v2, 0x1458, v71
	ds_write2_b32 v2, v24, v25 offset1:1
	v_add_u32_e32 v2, 0x1860, v71
	s_waitcnt vmcnt(9)
	ds_write2_b32 v2, v26, v27 offset1:1
	v_add_u32_e32 v2, 0x1868, v71
	ds_write2_b32 v2, v28, v29 offset1:1
	v_add_u32_e32 v2, 0x1c70, v71
	s_waitcnt vmcnt(8)
	ds_write2_b32 v2, v30, v31 offset1:1
	v_add_u32_e32 v2, 0x1c78, v71
	ds_write2_b32 v2, v32, v33 offset1:1
	v_add_u32_e32 v2, 0x2080, v71
	s_waitcnt vmcnt(7)
	ds_write2_b32 v2, v34, v35 offset1:1
	v_add_u32_e32 v2, 0x2088, v71
	ds_write2_b32 v2, v36, v37 offset1:1
	v_add_u32_e32 v2, 0x2490, v71
	s_waitcnt vmcnt(6)
; #define LAS __attribute__((address_space(3)))
; __device__ __forceinline__ unsigned pk2(float lo, float hi) { f32x2_cv_ v = {lo, hi}; return __builtin_bit_cast(unsigned, __builtin_convertvector(v, bf16x2_cv_)); }
; __device__ __forceinline__ void prep_item64(const float* W, int ldw, int srccol0, const float* g, bf16_t* dstrow0, int K, int k0, LAS float* scr, int lane) {
;     ...
;     for (int i = 0; i < 16; ++i) { const float gg = g ? g[k0 + 4 * i + kq] : 1.f; LAS float* d = scr + (4 * i + kq) * 65 + n4; d[0] = v[i][0] * gg; d[1] = v[i][1] * gg; d[2] = v[i][2] * gg; d[3] = v[i][3] * gg; }
;     asm volatile("s_waitcnt lgkmcnt(0)" ::: "memory");
;     const int c = lane & 7;
; #pragma unroll
;     for (int j = 0; j < 8; ++j) { const int n = (lane >> 3) + 8 * j; const LAS float* s = scr + (8 * c) * 65 + n;
;         u32x4 o; o.x = pk2(s[0 * 65], s[1 * 65]); o.y = pk2(s[2 * 65], s[3 * 65]); o.z = pk2(s[4 * 65], s[5 * 65]); o.w = pk2(s[6 * 65], s[7 * 65]);
;         *(u32x4*)(dstrow0 + (size_t)n * K + k0 + 8 * c) = o; }
;     asm volatile("s_waitcnt lgkmcnt(0)" ::: "memory");
	ds_write2_b32 v2, v38, v39 offset1:1
	v_add_u32_e32 v2, 0x2498, v71
	ds_write2_b32 v2, v40, v41 offset1:1
	v_add_u32_e32 v2, 0x28a0, v71
	s_waitcnt vmcnt(5)
	ds_write2_b32 v2, v42, v43 offset1:1
	v_add_u32_e32 v2, 0x28a8, v71
	ds_write2_b32 v2, v44, v45 offset1:1
	v_add_u32_e32 v2, 0x2cb0, v71
	s_waitcnt vmcnt(4)
	ds_write2_b32 v2, v46, v47 offset1:1
	v_add_u32_e32 v2, 0x2cb8, v71
	ds_write2_b32 v2, v48, v49 offset1:1
	v_add_u32_e32 v2, 0x30c0, v71
	s_waitcnt vmcnt(3)
	ds_write2_b32 v2, v50, v51 offset1:1
	v_add_u32_e32 v2, 0x30c8, v71
	ds_write2_b32 v2, v52, v53 offset1:1
	v_add_u32_e32 v2, 0x34d0, v71
	s_waitcnt vmcnt(2)
	ds_write2_b32 v2, v54, v55 offset1:1
	v_add_u32_e32 v2, 0x34d8, v71
	ds_write2_b32 v2, v56, v57 offset1:1
	v_add_u32_e32 v2, 0x38e0, v71
	s_waitcnt vmcnt(1)
	ds_write2_b32 v2, v58, v59 offset1:1
	v_add_u32_e32 v2, 0x38e8, v71
	ds_write2_b32 v2, v60, v61 offset1:1
	v_add_u32_e32 v2, 0x3cf0, v71
	s_waitcnt vmcnt(0)
	ds_write2_b32 v2, v62, v63 offset1:1
	v_add_u32_e32 v2, 0x3cf8, v71
	ds_write2_b32 v2, v64, v65 offset1:1
	s_waitcnt lgkmcnt(0)
	v_add_u32_e32 v26, 0x400, v115
	ds_read2_b32 v[6:7], v115 offset0:65 offset1:73
	ds_read2_b32 v[8:9], v115 offset1:8
	ds_read2_b32 v[10:11], v115 offset0:130 offset1:138
	ds_read2_b32 v[12:13], v115 offset0:195 offset1:203
	ds_read2_b32 v[14:15], v26 offset0:4 offset1:12
	ds_read2_b32 v[16:17], v26 offset0:69 offset1:77
	ds_read2_b32 v[18:19], v26 offset0:134 offset1:142
	ds_read2_b32 v[20:21], v26 offset0:199 offset1:207
	v_lshl_add_u64 v[2:3], s[4:5], 0, v[68:69]
	v_lshl_add_u64 v[22:23], v[2:3], 0, s[44:45]
	s_waitcnt lgkmcnt(0)
	v_cvt_pk_bf16_f32 v2, v8, v6
	v_cvt_pk_bf16_f32 v3, v10, v12
	v_cvt_pk_bf16_f32 v4, v14, v16
	v_cvt_pk_bf16_f32 v5, v18, v20
	v_lshl_add_u64 v[24:25], v[22:23], 0, v[72:73]
	global_store_dwordx4 v[24:25], v[2:5], off nt
	s_mov_b64 s[4:5], 0
	s_nop 0
	v_cvt_pk_bf16_f32 v2, v9, v7
	v_cvt_pk_bf16_f32 v3, v11, v13
	v_cvt_pk_bf16_f32 v4, v15, v17
	v_cvt_pk_bf16_f32 v5, v19, v21
	ds_read2_b32 v[8:9], v115 offset0:81 offset1:89
	ds_read2_b32 v[10:11], v115 offset0:16 offset1:24
	ds_read2_b32 v[12:13], v115 offset0:146 offset1:154
	ds_read2_b32 v[14:15], v115 offset0:211 offset1:219
	ds_read2_b32 v[16:17], v26 offset0:20 offset1:28
	ds_read2_b32 v[18:19], v26 offset0:85 offset1:93
	ds_read2_b32 v[20:21], v26 offset0:150 offset1:158
	ds_read2_b32 v[24:25], v26 offset0:215 offset1:223
	v_lshl_add_u64 v[6:7], v[22:23], 0, v[74:75]
	global_store_dwordx4 v[6:7], v[2:5], off nt
	v_lshl_add_u64 v[6:7], v[22:23], 0, v[76:77]
	s_waitcnt lgkmcnt(6)
	v_cvt_pk_bf16_f32 v2, v10, v8
	s_waitcnt lgkmcnt(4)
	v_cvt_pk_bf16_f32 v3, v12, v14
	s_waitcnt lgkmcnt(2)
	v_cvt_pk_bf16_f32 v4, v16, v18
	s_waitcnt lgkmcnt(0)
	v_cvt_pk_bf16_f32 v5, v20, v24
	global_store_dwordx4 v[6:7], v[2:5], off nt
	v_lshl_add_u64 v[6:7], v[22:23], 0, v[78:79]
	s_nop 0
	v_cvt_pk_bf16_f32 v2, v11, v9
	v_cvt_pk_bf16_f32 v3, v13, v15
	v_cvt_pk_bf16_f32 v4, v17, v19
	v_cvt_pk_bf16_f32 v5, v21, v25
	ds_read2_b32 v[8:9], v115 offset0:32 offset1:40
	ds_read2_b32 v[10:11], v115 offset0:97 offset1:105
	ds_read2_b32 v[12:13], v115 offset0:162 offset1:170
	ds_read2_b32 v[14:15], v115 offset0:227 offset1:235
	ds_read2_b32 v[16:17], v26 offset0:36 offset1:44
	ds_read2_b32 v[18:19], v26 offset0:101 offset1:109
	ds_read2_b32 v[20:21], v26 offset0:166 offset1:174
	ds_read2_b32 v[24:25], v26 offset0:231 offset1:239
	global_store_dwordx4 v[6:7], v[2:5], off nt
	v_lshl_add_u64 v[6:7], v[22:23], 0, v[80:81]
	s_waitcnt lgkmcnt(6)
	v_cvt_pk_bf16_f32 v2, v8, v10
	s_waitcnt lgkmcnt(4)
	v_cvt_pk_bf16_f32 v3, v12, v14
	s_waitcnt lgkmcnt(2)
	v_cvt_pk_bf16_f32 v4, v16, v18
	s_waitcnt lgkmcnt(0)
	v_cvt_pk_bf16_f32 v5, v20, v24
	global_store_dwordx4 v[6:7], v[2:5], off nt
	v_lshl_add_u64 v[6:7], v[22:23], 0, v[82:83]
	s_nop 0
	v_cvt_pk_bf16_f32 v2, v9, v11
	v_cvt_pk_bf16_f32 v3, v13, v15
	v_cvt_pk_bf16_f32 v4, v17, v19
	v_cvt_pk_bf16_f32 v5, v21, v25
	ds_read2_b32 v[8:9], v115 offset0:48 offset1:56
	ds_read2_b32 v[10:11], v115 offset0:113 offset1:121
	ds_read2_b32 v[12:13], v115 offset0:178 offset1:186
	ds_read2_b32 v[14:15], v115 offset0:243 offset1:251
	ds_read2_b32 v[16:17], v26 offset0:52 offset1:60
	ds_read2_b32 v[18:19], v26 offset0:117 offset1:125
	ds_read2_b32 v[20:21], v26 offset0:182 offset1:190
	ds_read2_b32 v[24:25], v26 offset0:247 offset1:255
	global_store_dwordx4 v[6:7], v[2:5], off nt
	v_lshl_add_u64 v[6:7], v[22:23], 0, v[84:85]
	s_waitcnt lgkmcnt(6)
	v_cvt_pk_bf16_f32 v2, v8, v10
	s_waitcnt lgkmcnt(4)
	v_cvt_pk_bf16_f32 v3, v12, v14
	s_waitcnt lgkmcnt(2)
	v_cvt_pk_bf16_f32 v4, v16, v18
	s_waitcnt lgkmcnt(0)
	v_cvt_pk_bf16_f32 v5, v20, v24
	global_store_dwordx4 v[6:7], v[2:5], off nt
	v_lshl_add_u64 v[6:7], v[22:23], 0, v[86:87]
	s_nop 0
	v_cvt_pk_bf16_f32 v2, v9, v11
	v_cvt_pk_bf16_f32 v3, v13, v15
	v_cvt_pk_bf16_f32 v4, v17, v19
	v_cvt_pk_bf16_f32 v5, v21, v25
	global_store_dwordx4 v[6:7], v[2:5], off nt
	s_waitcnt lgkmcnt(0)

; #define LAS __attribute__((address_space(3)))
; __device__ __forceinline__ unsigned pk2(float lo, float hi) { f32x2_cv_ v = {lo, hi}; return __builtin_bit_cast(unsigned, __builtin_convertvector(v, bf16x2_cv_)); }
; __device__ __forceinline__ void prep_item64(const float* W, int ldw, int srccol0, const float* g, bf16_t* dstrow0, int K, int k0, LAS float* scr, int lane) {
;     ...
;     for (int i = 0; i < 16; ++i) { const float gg = g ? g[k0 + 4 * i + kq] : 1.f; LAS float* d = scr + (4 * i + kq) * 65 + n4; d[0] = v[i][0] * gg; d[1] = v[i][1] * gg; d[2] = v[i][2] * gg; d[3] = v[i][3] * gg; }
;     asm volatile("s_waitcnt lgkmcnt(0)" ::: "memory");
;     const int c = lane & 7;
; #pragma unroll
;     for (int j = 0; j < 8; ++j) { const int n = (lane >> 3) + 8 * j; const LAS float* s = scr + (8 * c) * 65 + n;
;         u32x4 o; o.x = pk2(s[0 * 65], s[1 * 65]); o.y = pk2(s[2 * 65], s[3 * 65]); o.z = pk2(s[4 * 65], s[5 * 65]); o.w = pk2(s[6 * 65], s[7 * 65]);
;         *(u32x4*)(dstrow0 + (size_t)n * K + k0 + 8 * c) = o; }
;     asm volatile("s_waitcnt lgkmcnt(0)" ::: "memory");
; __device__ __forceinline__ void phase_prep_small(Frame& F) {
;     ...
;         if (r < I_PG) { const int kb = r / 16, n0 = (r % 16) * 64;
;             prep_item64(P.in[21] + (size_t)l * DM * DM, DM, n0, P.in[20] + l * DM, (bf16_t*)(wb + WSM_PG) + (size_t)n0 * DM, DM, kb * 64, scr, F.lane); continue; }
.LBB0_42:
	s_waitcnt vmcnt(0)
	v_pk_mul_f32 v[2:3], v[2:3], v[10:11] op_sel_hi:[1,0]
	v_add_u32_e32 v6, 0x3cf0, v71
	ds_write2_b32 v6, v2, v3 offset1:1
	v_pk_mul_f32 v[2:3], v[4:5], v[10:11] op_sel_hi:[1,0]
	v_add_u32_e32 v4, 0x3cf8, v71
	s_lshl_b32 s3, s3, 11
	ds_write2_b32 v4, v2, v3 offset1:1
	s_add_u32 s3, s68, s3
	s_waitcnt lgkmcnt(0)
	v_add_u32_e32 v26, 0x400, v115
	s_addc_u32 s5, s69, 0
	s_lshl_b32 s4, s36, 1
	ds_read2_b32 v[6:7], v115 offset0:65 offset1:73
	ds_read2_b32 v[8:9], v115 offset1:8
	ds_read2_b32 v[10:11], v115 offset0:130 offset1:138
	ds_read2_b32 v[12:13], v115 offset0:195 offset1:203
	ds_read2_b32 v[14:15], v26 offset0:4 offset1:12
	ds_read2_b32 v[16:17], v26 offset0:69 offset1:77
	ds_read2_b32 v[18:19], v26 offset0:134 offset1:142
	ds_read2_b32 v[20:21], v26 offset0:199 offset1:207
	s_add_u32 s4, s3, s4
	s_addc_u32 s5, s5, 0
	v_lshlrev_b32_e32 v68, 1, v70
	v_lshl_add_u64 v[2:3], s[4:5], 0, v[68:69]
	v_lshl_add_u64 v[22:23], v[2:3], 0, s[46:47]
	s_waitcnt lgkmcnt(0)
	v_cvt_pk_bf16_f32 v2, v8, v6
	v_cvt_pk_bf16_f32 v3, v10, v12
	v_cvt_pk_bf16_f32 v4, v14, v16
	v_cvt_pk_bf16_f32 v5, v18, v20
	v_lshl_add_u64 v[24:25], v[22:23], 0, v[88:89]
	global_store_dwordx4 v[24:25], v[2:5], off nt
	s_nop 1
	v_cvt_pk_bf16_f32 v2, v9, v7
	v_cvt_pk_bf16_f32 v3, v11, v13
	v_cvt_pk_bf16_f32 v4, v15, v17
	v_cvt_pk_bf16_f32 v5, v19, v21
	ds_read2_b32 v[8:9], v115 offset0:81 offset1:89
	ds_read2_b32 v[10:11], v115 offset0:16 offset1:24
	ds_read2_b32 v[12:13], v115 offset0:146 offset1:154
	ds_read2_b32 v[14:15], v115 offset0:211 offset1:219
	ds_read2_b32 v[16:17], v26 offset0:20 offset1:28
	ds_read2_b32 v[18:19], v26 offset0:85 offset1:93
	ds_read2_b32 v[20:21], v26 offset0:150 offset1:158
	ds_read2_b32 v[24:25], v26 offset0:215 offset1:223
	v_lshl_add_u64 v[6:7], v[22:23], 0, v[90:91]
	global_store_dwordx4 v[6:7], v[2:5], off nt
	v_lshl_add_u64 v[6:7], v[22:23], 0, v[92:93]
	s_waitcnt lgkmcnt(6)
	v_cvt_pk_bf16_f32 v2, v10, v8
	s_waitcnt lgkmcnt(4)
	v_cvt_pk_bf16_f32 v3, v12, v14
	s_waitcnt lgkmcnt(2)
	v_cvt_pk_bf16_f32 v4, v16, v18
	s_waitcnt lgkmcnt(0)
	v_cvt_pk_bf16_f32 v5, v20, v24
	global_store_dwordx4 v[6:7], v[2:5], off nt
	v_lshl_add_u64 v[6:7], v[22:23], 0, v[94:95]
	s_nop 0
	v_cvt_pk_bf16_f32 v2, v11, v9
	v_cvt_pk_bf16_f32 v3, v13, v15
	v_cvt_pk_bf16_f32 v4, v17, v19
	v_cvt_pk_bf16_f32 v5, v21, v25
	ds_read2_b32 v[8:9], v115 offset0:32 offset1:40
	ds_read2_b32 v[10:11], v115 offset0:97 offset1:105
	ds_read2_b32 v[12:13], v115 offset0:162 offset1:170
	ds_read2_b32 v[14:15], v115 offset0:227 offset1:235
	ds_read2_b32 v[16:17], v26 offset0:36 offset1:44
	ds_read2_b32 v[18:19], v26 offset0:101 offset1:109
	ds_read2_b32 v[20:21], v26 offset0:166 offset1:174
	ds_read2_b32 v[24:25], v26 offset0:231 offset1:239
	global_store_dwordx4 v[6:7], v[2:5], off nt
	v_lshl_add_u64 v[6:7], v[22:23], 0, v[96:97]
	s_waitcnt lgkmcnt(6)
	v_cvt_pk_bf16_f32 v2, v8, v10
	s_waitcnt lgkmcnt(4)
	v_cvt_pk_bf16_f32 v3, v12, v14
	s_waitcnt lgkmcnt(2)
	v_cvt_pk_bf16_f32 v4, v16, v18
	s_waitcnt lgkmcnt(0)
	v_cvt_pk_bf16_f32 v5, v20, v24
	global_store_dwordx4 v[6:7], v[2:5], off nt
	v_lshl_add_u64 v[6:7], v[22:23], 0, v[98:99]
	s_nop 0
	v_cvt_pk_bf16_f32 v2, v9, v11
	v_cvt_pk_bf16_f32 v3, v13, v15
	v_cvt_pk_bf16_f32 v4, v17, v19
	v_cvt_pk_bf16_f32 v5, v21, v25
	ds_read2_b32 v[8:9], v115 offset0:48 offset1:56
	ds_read2_b32 v[10:11], v115 offset0:113 offset1:121
	ds_read2_b32 v[12:13], v115 offset0:178 offset1:186
	ds_read2_b32 v[14:15], v115 offset0:243 offset1:251
	ds_read2_b32 v[16:17], v26 offset0:52 offset1:60
	ds_read2_b32 v[18:19], v26 offset0:117 offset1:125
	ds_read2_b32 v[20:21], v26 offset0:182 offset1:190
	ds_read2_b32 v[24:25], v26 offset0:247 offset1:255
	global_store_dwordx4 v[6:7], v[2:5], off nt
	v_lshl_add_u64 v[6:7], v[22:23], 0, v[100:101]
	s_waitcnt lgkmcnt(6)
	v_cvt_pk_bf16_f32 v2, v8, v10
	s_waitcnt lgkmcnt(4)
	v_cvt_pk_bf16_f32 v3, v12, v14
	s_waitcnt lgkmcnt(2)
	v_cvt_pk_bf16_f32 v4, v16, v18
	s_waitcnt lgkmcnt(0)
	v_cvt_pk_bf16_f32 v5, v20, v24
	global_store_dwordx4 v[6:7], v[2:5], off nt
	v_lshl_add_u64 v[6:7], v[22:23], 0, v[102:103]
	s_nop 0
	v_cvt_pk_bf16_f32 v2, v9, v11
	v_cvt_pk_bf16_f32 v3, v13, v15
	v_cvt_pk_bf16_f32 v4, v17, v19
	v_cvt_pk_bf16_f32 v5, v21, v25
	global_store_dwordx4 v[6:7], v[2:5], off nt
	s_waitcnt lgkmcnt(0)

; #define LAS __attribute__((address_space(3)))
; __device__ __forceinline__ unsigned pk2(float lo, float hi) { f32x2_cv_ v = {lo, hi}; return __builtin_bit_cast(unsigned, __builtin_convertvector(v, bf16x2_cv_)); }
; __device__ __forceinline__ void prep_item64(const float* W, int ldw, int srccol0, const float* g, bf16_t* dstrow0, int K, int k0, LAS float* scr, int lane) {
;     ...
;     for (int i = 0; i < 16; ++i) { const float gg = g ? g[k0 + 4 * i + kq] : 1.f; LAS float* d = scr + (4 * i + kq) * 65 + n4; d[0] = v[i][0] * gg; d[1] = v[i][1] * gg; d[2] = v[i][2] * gg; d[3] = v[i][3] * gg; }
;     asm volatile("s_waitcnt lgkmcnt(0)" ::: "memory");
;     const int c = lane & 7;
; #pragma unroll
;     for (int j = 0; j < 8; ++j) { const int n = (lane >> 3) + 8 * j; const LAS float* s = scr + (8 * c) * 65 + n;
;         u32x4 o; o.x = pk2(s[0 * 65], s[1 * 65]); o.y = pk2(s[2 * 65], s[3 * 65]); o.z = pk2(s[4 * 65], s[5 * 65]); o.w = pk2(s[6 * 65], s[7 * 65]);
;         *(u32x4*)(dstrow0 + (size_t)n * K + k0 + 8 * c) = o; }
;     asm volatile("s_waitcnt lgkmcnt(0)" ::: "memory");
; __device__ __forceinline__ void phase_prep_small(Frame& F) {
;     ...
;         if (r < I_OUT) { const int kb = r / 16, n0 = (r % 16) * 64; const int k0 = kb * 64;
;             const float* g = k0 < 512 ? P.in[9] + l * 512 : P.in[10] + l * 512 - 512;
;             prep_item64(P.in[11] + (size_t)l * DM * DM, DM, n0, g, (bf16_t*)(wb + WSM_OUT) + (size_t)n0 * DM, DM, k0, scr, F.lane); continue; }
.LBB0_69:
	s_waitcnt vmcnt(0)
	v_pk_mul_f32 v[2:3], v[2:3], v[10:11] op_sel_hi:[1,0]
	v_add_u32_e32 v6, 0x3cf0, v71
	ds_write2_b32 v6, v2, v3 offset1:1
	v_pk_mul_f32 v[2:3], v[4:5], v[10:11] op_sel_hi:[1,0]
	v_add_u32_e32 v4, 0x3cf8, v71
	s_lshl_b32 s4, s36, 11
	ds_write2_b32 v4, v2, v3 offset1:1
	s_add_u32 s4, s68, s4
	s_waitcnt lgkmcnt(0)
	v_add_u32_e32 v26, 0x400, v115
	s_addc_u32 s5, s69, 0
	s_lshl_b32 s3, s3, 1
	ds_read2_b32 v[6:7], v115 offset0:65 offset1:73
	ds_read2_b32 v[8:9], v115 offset1:8
	ds_read2_b32 v[10:11], v115 offset0:130 offset1:138
	ds_read2_b32 v[12:13], v115 offset0:195 offset1:203
	ds_read2_b32 v[14:15], v26 offset0:4 offset1:12
	ds_read2_b32 v[16:17], v26 offset0:69 offset1:77
	ds_read2_b32 v[18:19], v26 offset0:134 offset1:142
	ds_read2_b32 v[20:21], v26 offset0:199 offset1:207
	s_add_u32 s4, s4, s3
	s_addc_u32 s5, s5, 0
	v_lshlrev_b32_e32 v68, 1, v70
	v_lshl_add_u64 v[2:3], s[4:5], 0, v[68:69]
	v_lshl_add_u64 v[22:23], v[2:3], 0, s[48:49]
	s_waitcnt lgkmcnt(6)
	v_cvt_pk_bf16_f32 v2, v8, v6
	s_waitcnt lgkmcnt(4)
	v_cvt_pk_bf16_f32 v3, v10, v12
	s_waitcnt lgkmcnt(2)
	v_cvt_pk_bf16_f32 v4, v14, v16
	s_waitcnt lgkmcnt(0)
	v_cvt_pk_bf16_f32 v5, v18, v20
	v_lshl_add_u64 v[24:25], v[22:23], 0, v[88:89]
	global_store_dwordx4 v[24:25], v[2:5], off nt
	s_nop 1
	v_cvt_pk_bf16_f32 v2, v9, v7
	v_cvt_pk_bf16_f32 v3, v11, v13
	v_cvt_pk_bf16_f32 v4, v15, v17
	v_cvt_pk_bf16_f32 v5, v19, v21
	ds_read2_b32 v[8:9], v115 offset0:81 offset1:89
	ds_read2_b32 v[10:11], v115 offset0:16 offset1:24
	ds_read2_b32 v[12:13], v115 offset0:146 offset1:154
	ds_read2_b32 v[14:15], v115 offset0:211 offset1:219
	ds_read2_b32 v[16:17], v26 offset0:20 offset1:28
	ds_read2_b32 v[18:19], v26 offset0:85 offset1:93
	ds_read2_b32 v[20:21], v26 offset0:150 offset1:158
	ds_read2_b32 v[24:25], v26 offset0:215 offset1:223
	v_lshl_add_u64 v[6:7], v[22:23], 0, v[90:91]
	global_store_dwordx4 v[6:7], v[2:5], off nt
	v_lshl_add_u64 v[6:7], v[22:23], 0, v[92:93]
	s_waitcnt lgkmcnt(6)
	v_cvt_pk_bf16_f32 v2, v10, v8
	s_waitcnt lgkmcnt(4)
	v_cvt_pk_bf16_f32 v3, v12, v14
	s_waitcnt lgkmcnt(2)
	v_cvt_pk_bf16_f32 v4, v16, v18
	s_waitcnt lgkmcnt(0)
	v_cvt_pk_bf16_f32 v5, v20, v24
	global_store_dwordx4 v[6:7], v[2:5], off nt
	v_lshl_add_u64 v[6:7], v[22:23], 0, v[94:95]
	s_nop 0
	v_cvt_pk_bf16_f32 v2, v11, v9
	v_cvt_pk_bf16_f32 v3, v13, v15
	v_cvt_pk_bf16_f32 v4, v17, v19
	v_cvt_pk_bf16_f32 v5, v21, v25
	ds_read2_b32 v[8:9], v115 offset0:32 offset1:40
	ds_read2_b32 v[10:11], v115 offset0:97 offset1:105
	ds_read2_b32 v[12:13], v115 offset0:162 offset1:170
	ds_read2_b32 v[14:15], v115 offset0:227 offset1:235
	ds_read2_b32 v[16:17], v26 offset0:36 offset1:44
	ds_read2_b32 v[18:19], v26 offset0:101 offset1:109
	ds_read2_b32 v[20:21], v26 offset0:166 offset1:174
	ds_read2_b32 v[24:25], v26 offset0:231 offset1:239
	global_store_dwordx4 v[6:7], v[2:5], off nt
	v_lshl_add_u64 v[6:7], v[22:23], 0, v[96:97]
	s_waitcnt lgkmcnt(6)
	v_cvt_pk_bf16_f32 v2, v8, v10
	s_waitcnt lgkmcnt(4)
	v_cvt_pk_bf16_f32 v3, v12, v14
	s_waitcnt lgkmcnt(2)
	v_cvt_pk_bf16_f32 v4, v16, v18
	s_waitcnt lgkmcnt(0)
	v_cvt_pk_bf16_f32 v5, v20, v24
	global_store_dwordx4 v[6:7], v[2:5], off nt
	v_lshl_add_u64 v[6:7], v[22:23], 0, v[98:99]
	s_nop 0
	v_cvt_pk_bf16_f32 v2, v9, v11
	v_cvt_pk_bf16_f32 v3, v13, v15
	v_cvt_pk_bf16_f32 v4, v17, v19
	v_cvt_pk_bf16_f32 v5, v21, v25
	ds_read2_b32 v[8:9], v115 offset0:48 offset1:56
	ds_read2_b32 v[10:11], v115 offset0:113 offset1:121
	ds_read2_b32 v[12:13], v115 offset0:178 offset1:186
	ds_read2_b32 v[14:15], v115 offset0:243 offset1:251
	ds_read2_b32 v[16:17], v26 offset0:52 offset1:60
	ds_read2_b32 v[18:19], v26 offset0:117 offset1:125
	ds_read2_b32 v[20:21], v26 offset0:182 offset1:190
	ds_read2_b32 v[24:25], v26 offset0:247 offset1:255
	global_store_dwordx4 v[6:7], v[2:5], off nt
	v_lshl_add_u64 v[6:7], v[22:23], 0, v[100:101]
	s_waitcnt lgkmcnt(6)
	v_cvt_pk_bf16_f32 v2, v8, v10
	s_waitcnt lgkmcnt(4)
	v_cvt_pk_bf16_f32 v3, v12, v14
	s_waitcnt lgkmcnt(2)
	v_cvt_pk_bf16_f32 v4, v16, v18
	s_waitcnt lgkmcnt(0)
	v_cvt_pk_bf16_f32 v5, v20, v24
	global_store_dwordx4 v[6:7], v[2:5], off nt
	v_lshl_add_u64 v[6:7], v[22:23], 0, v[102:103]
	s_nop 0
	v_cvt_pk_bf16_f32 v2, v9, v11
	v_cvt_pk_bf16_f32 v3, v13, v15
	v_cvt_pk_bf16_f32 v4, v17, v19
	v_cvt_pk_bf16_f32 v5, v21, v25
	global_store_dwordx4 v[6:7], v[2:5], off nt
	s_waitcnt lgkmcnt(0)

; #define LAS __attribute__((address_space(3)))
; __device__ __forceinline__ unsigned pk2(float lo, float hi) { f32x2_cv_ v = {lo, hi}; return __builtin_bit_cast(unsigned, __builtin_convertvector(v, bf16x2_cv_)); }
; __device__ __forceinline__ void prep_item64(const float* W, int ldw, int srccol0, const float* g, bf16_t* dstrow0, int K, int k0, LAS float* scr, int lane) {
;     ...
;     for (int i = 0; i < 16; ++i) { const float gg = g ? g[k0 + 4 * i + kq] : 1.f; LAS float* d = scr + (4 * i + kq) * 65 + n4; d[0] = v[i][0] * gg; d[1] = v[i][1] * gg; d[2] = v[i][2] * gg; d[3] = v[i][3] * gg; }
;     asm volatile("s_waitcnt lgkmcnt(0)" ::: "memory");
;     const int c = lane & 7;
; #pragma unroll
;     for (int j = 0; j < 8; ++j) { const int n = (lane >> 3) + 8 * j; const LAS float* s = scr + (8 * c) * 65 + n;
;         u32x4 o; o.x = pk2(s[0 * 65], s[1 * 65]); o.y = pk2(s[2 * 65], s[3 * 65]); o.z = pk2(s[4 * 65], s[5 * 65]); o.w = pk2(s[6 * 65], s[7 * 65]);
;         *(u32x4*)(dstrow0 + (size_t)n * K + k0 + 8 * c) = o; }
;     asm volatile("s_waitcnt lgkmcnt(0)" ::: "memory");
; __device__ __forceinline__ void phase_prep_small(Frame& F) {
;     ...
;         r -= I_UQ;
;         if (r < I_UKV) { const int kb = r / 16, n0 = (r % 16) * 64; const int hh = (n0 & 511) >> 6; const int src = hh * 128 + (n0 >= 512 ? 64 : 0);
;             prep_item64(P.in[8] + (size_t)l * KVRANK * 1024, 1024, src, P.in[7] + l * KVRANK, (bf16_t*)(wb + WSM_UKV) + (size_t)n0 * KVRANK, KVRANK, kb * 64, scr, F.lane); continue; }
.LBB0_96:
	s_waitcnt vmcnt(0)
	v_pk_mul_f32 v[2:3], v[2:3], v[10:11] op_sel_hi:[1,0]
	v_add_u32_e32 v6, 0x3cf0, v71
	s_lshl_b32 s3, s3, 15
	ds_write2_b32 v6, v2, v3 offset1:1
	v_pk_mul_f32 v[2:3], v[4:5], v[10:11] op_sel_hi:[1,0]
	v_add_u32_e32 v4, 0x3cf8, v71
	s_and_b32 s3, s3, 0x78000
	ds_write2_b32 v4, v2, v3 offset1:1
	s_add_u32 s3, s68, s3
	s_waitcnt lgkmcnt(0)
	v_add_u32_e32 v26, 0x400, v115
	s_addc_u32 s5, s69, 0
	s_lshl_b32 s4, s36, 1
	ds_read2_b32 v[6:7], v115 offset0:65 offset1:73
	ds_read2_b32 v[8:9], v115 offset1:8
	ds_read2_b32 v[10:11], v115 offset0:130 offset1:138
	ds_read2_b32 v[12:13], v115 offset0:195 offset1:203
	ds_read2_b32 v[14:15], v26 offset0:4 offset1:12
	ds_read2_b32 v[16:17], v26 offset0:69 offset1:77
	ds_read2_b32 v[18:19], v26 offset0:134 offset1:142
	ds_read2_b32 v[20:21], v26 offset0:199 offset1:207
	s_add_u32 s4, s3, s4
	s_addc_u32 s5, s5, 0
	v_lshlrev_b32_e32 v68, 1, v70
	v_lshl_add_u64 v[2:3], s[4:5], 0, v[68:69]
	v_lshl_add_u64 v[22:23], v[2:3], 0, s[50:51]
	s_waitcnt lgkmcnt(0)
	v_cvt_pk_bf16_f32 v2, v8, v6
	v_cvt_pk_bf16_f32 v3, v10, v12
	v_cvt_pk_bf16_f32 v4, v14, v16
	v_cvt_pk_bf16_f32 v5, v18, v20
	v_lshl_add_u64 v[24:25], v[22:23], 0, v[72:73]
	global_store_dwordx4 v[24:25], v[2:5], off nt
	s_nop 1
	v_cvt_pk_bf16_f32 v2, v9, v7
	v_cvt_pk_bf16_f32 v3, v11, v13
	v_cvt_pk_bf16_f32 v4, v15, v17
	v_cvt_pk_bf16_f32 v5, v19, v21
	ds_read2_b32 v[8:9], v115 offset0:81 offset1:89
	ds_read2_b32 v[10:11], v115 offset0:16 offset1:24
	ds_read2_b32 v[12:13], v115 offset0:146 offset1:154
	ds_read2_b32 v[14:15], v115 offset0:211 offset1:219
	ds_read2_b32 v[16:17], v26 offset0:20 offset1:28
	ds_read2_b32 v[18:19], v26 offset0:85 offset1:93
	ds_read2_b32 v[20:21], v26 offset0:150 offset1:158
	ds_read2_b32 v[24:25], v26 offset0:215 offset1:223
	v_lshl_add_u64 v[6:7], v[22:23], 0, v[74:75]
	global_store_dwordx4 v[6:7], v[2:5], off nt
	v_lshl_add_u64 v[6:7], v[22:23], 0, v[76:77]
	s_waitcnt lgkmcnt(6)
	v_cvt_pk_bf16_f32 v2, v10, v8
	s_waitcnt lgkmcnt(4)
	v_cvt_pk_bf16_f32 v3, v12, v14
	s_waitcnt lgkmcnt(2)
	v_cvt_pk_bf16_f32 v4, v16, v18
	s_waitcnt lgkmcnt(0)
	v_cvt_pk_bf16_f32 v5, v20, v24
	global_store_dwordx4 v[6:7], v[2:5], off nt
	v_lshl_add_u64 v[6:7], v[22:23], 0, v[78:79]
	s_nop 0
	v_cvt_pk_bf16_f32 v2, v11, v9
	v_cvt_pk_bf16_f32 v3, v13, v15
	v_cvt_pk_bf16_f32 v4, v17, v19
	v_cvt_pk_bf16_f32 v5, v21, v25
	ds_read2_b32 v[8:9], v115 offset0:32 offset1:40
	ds_read2_b32 v[10:11], v115 offset0:97 offset1:105
	ds_read2_b32 v[12:13], v115 offset0:162 offset1:170
	ds_read2_b32 v[14:15], v115 offset0:227 offset1:235
	ds_read2_b32 v[16:17], v26 offset0:36 offset1:44
	ds_read2_b32 v[18:19], v26 offset0:101 offset1:109
	ds_read2_b32 v[20:21], v26 offset0:166 offset1:174
	ds_read2_b32 v[24:25], v26 offset0:231 offset1:239
	global_store_dwordx4 v[6:7], v[2:5], off nt
	v_lshl_add_u64 v[6:7], v[22:23], 0, v[80:81]
	s_waitcnt lgkmcnt(6)
	v_cvt_pk_bf16_f32 v2, v8, v10
	s_waitcnt lgkmcnt(4)
	v_cvt_pk_bf16_f32 v3, v12, v14
	s_waitcnt lgkmcnt(2)
	v_cvt_pk_bf16_f32 v4, v16, v18
	s_waitcnt lgkmcnt(0)
	v_cvt_pk_bf16_f32 v5, v20, v24
	global_store_dwordx4 v[6:7], v[2:5], off nt
	v_lshl_add_u64 v[6:7], v[22:23], 0, v[82:83]
	s_nop 0
	v_cvt_pk_bf16_f32 v2, v9, v11
	v_cvt_pk_bf16_f32 v3, v13, v15
	v_cvt_pk_bf16_f32 v4, v17, v19
	v_cvt_pk_bf16_f32 v5, v21, v25
	ds_read2_b32 v[8:9], v115 offset0:48 offset1:56
	ds_read2_b32 v[10:11], v115 offset0:113 offset1:121
	ds_read2_b32 v[12:13], v115 offset0:178 offset1:186
	ds_read2_b32 v[14:15], v115 offset0:243 offset1:251
	ds_read2_b32 v[16:17], v26 offset0:52 offset1:60
	ds_read2_b32 v[18:19], v26 offset0:117 offset1:125
	ds_read2_b32 v[20:21], v26 offset0:182 offset1:190
	ds_read2_b32 v[24:25], v26 offset0:247 offset1:255
	global_store_dwordx4 v[6:7], v[2:5], off nt
	v_lshl_add_u64 v[6:7], v[22:23], 0, v[84:85]
	s_waitcnt lgkmcnt(6)
	v_cvt_pk_bf16_f32 v2, v8, v10
	s_waitcnt lgkmcnt(4)
	v_cvt_pk_bf16_f32 v3, v12, v14
	s_waitcnt lgkmcnt(2)
	v_cvt_pk_bf16_f32 v4, v16, v18
	s_waitcnt lgkmcnt(0)
	v_cvt_pk_bf16_f32 v5, v20, v24
	global_store_dwordx4 v[6:7], v[2:5], off nt
	v_lshl_add_u64 v[6:7], v[22:23], 0, v[86:87]
	s_nop 0
	v_cvt_pk_bf16_f32 v2, v9, v11
	v_cvt_pk_bf16_f32 v3, v13, v15
	v_cvt_pk_bf16_f32 v4, v17, v19
	v_cvt_pk_bf16_f32 v5, v21, v25
	global_store_dwordx4 v[6:7], v[2:5], off nt
	s_waitcnt lgkmcnt(0)

; #define LAS __attribute__((address_space(3)))
; __device__ __forceinline__ unsigned pk2(float lo, float hi) { f32x2_cv_ v = {lo, hi}; return __builtin_bit_cast(unsigned, __builtin_convertvector(v, bf16x2_cv_)); }
; __device__ __forceinline__ void prep_item64(const float* W, int ldw, int srccol0, const float* g, bf16_t* dstrow0, int K, int k0, LAS float* scr, int lane) {
;     ...
;     for (int i = 0; i < 16; ++i) { const float gg = g ? g[k0 + 4 * i + kq] : 1.f; LAS float* d = scr + (4 * i + kq) * 65 + n4; d[0] = v[i][0] * gg; d[1] = v[i][1] * gg; d[2] = v[i][2] * gg; d[3] = v[i][3] * gg; }
;     asm volatile("s_waitcnt lgkmcnt(0)" ::: "memory");
;     const int c = lane & 7;
; #pragma unroll
;     for (int j = 0; j < 8; ++j) { const int n = (lane >> 3) + 8 * j; const LAS float* s = scr + (8 * c) * 65 + n;
;         u32x4 o; o.x = pk2(s[0 * 65], s[1 * 65]); o.y = pk2(s[2 * 65], s[3 * 65]); o.z = pk2(s[4 * 65], s[5 * 65]); o.w = pk2(s[6 * 65], s[7 * 65]);
;         *(u32x4*)(dstrow0 + (size_t)n * K + k0 + 8 * c) = o; }
;     asm volatile("s_waitcnt lgkmcnt(0)" ::: "memory");
; __device__ __forceinline__ void phase_prep_small(Frame& F) {
;     ...
;         if (r < I_UQ) { const int kb = r / 12, n0 = (r % 12) * 64;
;             prep_item64(P.in[6] + (size_t)l * QRANK * 768, 768, n0, P.in[5] + l * QRANK, (bf16_t*)(wb + WSM_UQ) + (size_t)n0 * QRANK, QRANK, kb * 64, scr, F.lane); continue; }
.LBB0_123:
	s_waitcnt vmcnt(0)
	v_pk_mul_f32 v[2:3], v[2:3], v[10:11] op_sel_hi:[1,0]
	v_add_u32_e32 v6, 0x3cf0, v71
	ds_write2_b32 v6, v2, v3 offset1:1
	v_pk_mul_f32 v[2:3], v[4:5], v[10:11] op_sel_hi:[1,0]
	v_add_u32_e32 v4, 0x3cf8, v71
	s_mul_i32 s3, s3, 0xc000
	ds_write2_b32 v4, v2, v3 offset1:1
	s_add_u32 s3, s68, s3
	s_waitcnt lgkmcnt(0)
	v_add_u32_e32 v28, 0x400, v115
	s_addc_u32 s5, s69, 0
	s_lshl_b32 s4, s36, 1
	ds_read2_b32 v[6:7], v115 offset0:65 offset1:73
	ds_read2_b32 v[8:9], v115 offset1:8
	ds_read2_b32 v[10:11], v115 offset0:130 offset1:138
	ds_read2_b32 v[12:13], v115 offset0:195 offset1:203
	ds_read2_b32 v[14:15], v28 offset0:4 offset1:12
	ds_read2_b32 v[16:17], v28 offset0:69 offset1:77
	ds_read2_b32 v[18:19], v28 offset0:134 offset1:142
	ds_read2_b32 v[20:21], v28 offset0:199 offset1:207
	s_add_u32 s4, s3, s4
	s_addc_u32 s5, s5, 0
	v_lshlrev_b32_e32 v68, 1, v70
	v_lshl_add_u64 v[2:3], s[4:5], 0, v[68:69]
	v_lshl_add_u64 v[22:23], v[2:3], 0, s[52:53]
	s_waitcnt lgkmcnt(0)
	v_cvt_pk_bf16_f32 v2, v8, v6
	v_cvt_pk_bf16_f32 v3, v10, v12
	v_cvt_pk_bf16_f32 v4, v14, v16
	v_cvt_pk_bf16_f32 v5, v18, v20
	v_lshl_add_u64 v[24:25], v[22:23], 0, v[104:105]
	global_store_dwordx4 v[24:25], v[2:5], off nt
	v_add_co_u32_e32 v6, vcc, s63, v24
	s_nop 0
	v_cvt_pk_bf16_f32 v2, v9, v7
	v_cvt_pk_bf16_f32 v3, v11, v13
	v_cvt_pk_bf16_f32 v4, v15, v17
	v_cvt_pk_bf16_f32 v5, v19, v21
	ds_read2_b32 v[8:9], v115 offset0:81 offset1:89
	ds_read2_b32 v[10:11], v115 offset0:16 offset1:24
	ds_read2_b32 v[12:13], v115 offset0:146 offset1:154
	ds_read2_b32 v[14:15], v115 offset0:211 offset1:219
	ds_read2_b32 v[16:17], v28 offset0:20 offset1:28
	ds_read2_b32 v[18:19], v28 offset0:85 offset1:93
	ds_read2_b32 v[20:21], v28 offset0:150 offset1:158
	ds_read2_b32 v[26:27], v28 offset0:215 offset1:223
	v_addc_co_u32_e32 v7, vcc, 0, v25, vcc
	global_store_dwordx4 v[6:7], v[2:5], off offset:2048 nt
	v_add_co_u32_e32 v6, vcc, s64, v24
	s_waitcnt lgkmcnt(6)
	v_cvt_pk_bf16_f32 v2, v10, v8
	s_waitcnt lgkmcnt(4)
	v_cvt_pk_bf16_f32 v3, v12, v14
	s_waitcnt lgkmcnt(2)
	v_cvt_pk_bf16_f32 v4, v16, v18
	s_waitcnt lgkmcnt(0)
	v_cvt_pk_bf16_f32 v5, v20, v26
	v_addc_co_u32_e32 v7, vcc, 0, v25, vcc
	global_store_dwordx4 v[6:7], v[2:5], off nt
	v_add_co_u32_e32 v6, vcc, s65, v24
	s_nop 0
	v_cvt_pk_bf16_f32 v2, v11, v9
	v_cvt_pk_bf16_f32 v3, v13, v15
	v_cvt_pk_bf16_f32 v4, v17, v19
	v_cvt_pk_bf16_f32 v5, v21, v27
	v_addc_co_u32_e32 v7, vcc, 0, v25, vcc
	ds_read2_b32 v[8:9], v115 offset0:32 offset1:40
	ds_read2_b32 v[10:11], v115 offset0:97 offset1:105
	ds_read2_b32 v[12:13], v115 offset0:162 offset1:170
	ds_read2_b32 v[14:15], v115 offset0:227 offset1:235
	ds_read2_b32 v[16:17], v28 offset0:36 offset1:44
	ds_read2_b32 v[18:19], v28 offset0:101 offset1:109
	ds_read2_b32 v[20:21], v28 offset0:166 offset1:174
	ds_read2_b32 v[24:25], v28 offset0:231 offset1:239
	global_store_dwordx4 v[6:7], v[2:5], off offset:2048 nt
	v_lshl_add_u64 v[6:7], v[22:23], 0, v[106:107]
	s_waitcnt lgkmcnt(6)
	v_cvt_pk_bf16_f32 v2, v8, v10
	s_waitcnt lgkmcnt(4)
	v_cvt_pk_bf16_f32 v3, v12, v14
	s_waitcnt lgkmcnt(2)
	v_cvt_pk_bf16_f32 v4, v16, v18
	s_waitcnt lgkmcnt(0)
	v_cvt_pk_bf16_f32 v5, v20, v24
	global_store_dwordx4 v[6:7], v[2:5], off nt
	v_lshl_add_u64 v[6:7], v[22:23], 0, v[108:109]
	s_nop 0
	v_cvt_pk_bf16_f32 v2, v9, v11
	v_cvt_pk_bf16_f32 v3, v13, v15
	v_cvt_pk_bf16_f32 v4, v17, v19
	v_cvt_pk_bf16_f32 v5, v21, v25
	ds_read2_b32 v[8:9], v115 offset0:48 offset1:56
	ds_read2_b32 v[10:11], v115 offset0:113 offset1:121
	ds_read2_b32 v[12:13], v115 offset0:178 offset1:186
	ds_read2_b32 v[14:15], v115 offset0:243 offset1:251
	ds_read2_b32 v[16:17], v28 offset0:52 offset1:60
	ds_read2_b32 v[18:19], v28 offset0:117 offset1:125
	ds_read2_b32 v[20:21], v28 offset0:182 offset1:190
	ds_read2_b32 v[24:25], v28 offset0:247 offset1:255
	global_store_dwordx4 v[6:7], v[2:5], off nt
	v_lshl_add_u64 v[6:7], v[22:23], 0, v[110:111]
	s_waitcnt lgkmcnt(6)
	v_cvt_pk_bf16_f32 v2, v8, v10
	s_waitcnt lgkmcnt(4)
	v_cvt_pk_bf16_f32 v3, v12, v14
	s_waitcnt lgkmcnt(2)
	v_cvt_pk_bf16_f32 v4, v16, v18
	s_waitcnt lgkmcnt(0)
	v_cvt_pk_bf16_f32 v5, v20, v24
	global_store_dwordx4 v[6:7], v[2:5], off nt
	v_lshl_add_u64 v[6:7], v[22:23], 0, v[112:113]
	s_nop 0
	v_cvt_pk_bf16_f32 v2, v9, v11
	v_cvt_pk_bf16_f32 v3, v13, v15
	v_cvt_pk_bf16_f32 v4, v17, v19
	v_cvt_pk_bf16_f32 v5, v21, v25
	global_store_dwordx4 v[6:7], v[2:5], off nt
	s_waitcnt lgkmcnt(0)

; #define LAS __attribute__((address_space(3)))
; __device__ __forceinline__ unsigned pk2(float lo, float hi) { f32x2_cv_ v = {lo, hi}; return __builtin_bit_cast(unsigned, __builtin_convertvector(v, bf16x2_cv_)); }
; __device__ __forceinline__ void prep_item(const float* W, int ldw, int srccol0, const float* g, bf16_t* dstrow0, int K, int k0, LAS float* scr, int lane) {
;     const int c = lane & 7;
;     if (srccol0 < 0) {
; #pragma unroll
;         for (int j = 0; j < 4; ++j) { const int n = (lane >> 3) + 8 * j; *(u32x4*)(dstrow0 + (size_t)n * K + k0 + 8 * c) = (u32x4){0u, 0u, 0u, 0u}; }
;         return;
;     }
; #pragma unroll 8
;     for (int i = 0; i < 32; ++i) { const int kk = 2 * i + (lane >> 5); float v = W[(size_t)(k0 + kk) * ldw + srccol0 + (lane & 31)]; if (g) v *= g[k0 + kk]; scr[kk * 33 + (lane & 31)] = v; }
;     asm volatile("s_waitcnt lgkmcnt(0)" ::: "memory");
; #pragma unroll
;     for (int j = 0; j < 4; ++j) { const int n = (lane >> 3) + 8 * j; const LAS float* s = scr + (8 * c) * 33 + n;
;         u32x4 o; o.x = pk2(s[0 * 33], s[1 * 33]); o.y = pk2(s[2 * 33], s[3 * 33]); o.z = pk2(s[4 * 33], s[5 * 33]); o.w = pk2(s[6 * 33], s[7 * 33]);
;         *(u32x4*)(dstrow0 + (size_t)n * K + k0 + 8 * c) = o; }
;     asm volatile("s_waitcnt lgkmcnt(0)" ::: "memory");
; __device__ __forceinline__ void phase_prep_small(Frame& F) {
;     ...
;         if (r < I_INT) { const int kb = r / 4, n0 = 2176 + (r % 4) * 32; const int src = n0 < 2208 ? n0 : -1;
;             prep_item(P.in[4] + (size_t)l * DM * INC, INC, src, P.in[3] + l * DM, (bf16_t*)(wb + WSM_IN) + (size_t)n0 * DM, DM, kb * 64, scr, F.lane); continue; }
.LBB0_145:
	s_waitcnt lgkmcnt(0)
	ds_read2_b32 v[6:7], v119 offset0:33 offset1:41
	ds_read2_b32 v[8:9], v119 offset1:8
	ds_read2_b32 v[10:11], v119 offset0:66 offset1:74
	ds_read2_b32 v[12:13], v119 offset0:99 offset1:107
	ds_read2_b32 v[14:15], v119 offset0:132 offset1:140
	ds_read2_b32 v[16:17], v119 offset0:165 offset1:173
	ds_read2_b32 v[18:19], v119 offset0:198 offset1:206
	ds_read2_b32 v[20:21], v119 offset0:231 offset1:239
	s_lshl_b64 s[4:5], s[36:37], 1
	s_add_u32 s4, s3, s4
	s_addc_u32 s5, s55, s5
	v_lshlrev_b32_e32 v68, 1, v118
	v_lshl_add_u64 v[22:23], s[4:5], 0, v[68:69]
	s_waitcnt lgkmcnt(0)
	v_cvt_pk_bf16_f32 v2, v8, v6
	v_cvt_pk_bf16_f32 v3, v10, v12
	v_cvt_pk_bf16_f32 v4, v14, v16
	v_cvt_pk_bf16_f32 v5, v18, v20
	v_lshl_add_u64 v[24:25], v[22:23], 0, v[88:89]
	global_store_dwordx4 v[24:25], v[2:5], off nt
	s_mov_b64 s[4:5], 0
	s_nop 0
	v_cvt_pk_bf16_f32 v2, v9, v7
	v_cvt_pk_bf16_f32 v3, v11, v13
	v_cvt_pk_bf16_f32 v4, v15, v17
	v_cvt_pk_bf16_f32 v5, v19, v21
	ds_read2_b32 v[8:9], v119 offset0:49 offset1:57
	ds_read2_b32 v[10:11], v119 offset0:16 offset1:24
	ds_read2_b32 v[12:13], v119 offset0:82 offset1:90
	ds_read2_b32 v[14:15], v119 offset0:115 offset1:123
	ds_read2_b32 v[16:17], v119 offset0:148 offset1:156
	ds_read2_b32 v[18:19], v119 offset0:181 offset1:189
	ds_read2_b32 v[20:21], v119 offset0:214 offset1:222
	ds_read2_b32 v[24:25], v119 offset0:247 offset1:255
	v_lshl_add_u64 v[6:7], v[22:23], 0, v[90:91]
	global_store_dwordx4 v[6:7], v[2:5], off nt
	v_lshl_add_u64 v[6:7], v[22:23], 0, v[92:93]
	s_waitcnt lgkmcnt(6)
	v_cvt_pk_bf16_f32 v2, v10, v8
	s_waitcnt lgkmcnt(4)
	v_cvt_pk_bf16_f32 v3, v12, v14
	s_waitcnt lgkmcnt(2)
	v_cvt_pk_bf16_f32 v4, v16, v18
	s_waitcnt lgkmcnt(0)
	v_cvt_pk_bf16_f32 v5, v20, v24
	global_store_dwordx4 v[6:7], v[2:5], off nt
	v_lshl_add_u64 v[6:7], v[22:23], 0, v[94:95]
	s_nop 0
	v_cvt_pk_bf16_f32 v2, v11, v9
	v_cvt_pk_bf16_f32 v3, v13, v15
	v_cvt_pk_bf16_f32 v4, v17, v19
	v_cvt_pk_bf16_f32 v5, v21, v25
	global_store_dwordx4 v[6:7], v[2:5], off nt
	s_waitcnt lgkmcnt(0)
.LBB0_146:
	s_and_b64 vcc, exec, s[4:5]
	s_cbranch_vccz .LBB0_148
	s_lshl_b64 s[4:5], s[36:37], 1
	s_add_u32 s4, s3, s4
	s_addc_u32 s5, s55, s5
	v_lshlrev_b32_e32 v68, 1, v118
	v_lshl_add_u64 v[2:3], s[4:5], 0, v[68:69]
	v_lshl_add_u64 v[2:3], v[2:3], 0, v[88:89]
	s_mov_b32 s36, s37
	s_mov_b32 s38, s37
	s_mov_b32 s39, s37
	v_mov_b64_e32 v[6:7], s[36:37]
	v_add_co_u32_e32 v4, vcc, 0x4000, v2
	v_mov_b64_e32 v[8:9], s[38:39]
	s_nop 0
	v_addc_co_u32_e32 v5, vcc, 0, v3, vcc
	global_store_dwordx4 v[4:5], v[6:9], off nt
	v_add_co_u32_e32 v4, vcc, 0x8000, v2
	global_store_dwordx4 v[2:3], v[6:9], off nt
	s_nop 0
	v_addc_co_u32_e32 v5, vcc, 0, v3, vcc
	v_add_co_u32_e32 v2, vcc, 0xc000, v2
	global_store_dwordx4 v[4:5], v[6:9], off nt
	s_nop 0
	v_addc_co_u32_e32 v3, vcc, 0, v3, vcc
	global_store_dwordx4 v[2:3], v[6:9], off nt
